# code placement: whole instruction stream shifted by 4 bytes (one s_nop at entry) relative to the best version
# baseline (speedup 1.0000x reference)
; #define LAS __attribute__((address_space(3)))
; __global__ void __launch_bounds__(NTHR, 2) fwd(Args args) {
;     ...
;     F.lds = (LAS unsigned char*)lds; F.glds = lds; F.ws = args.ws; F.ctl = (unsigned*)(args.ws + WS_CTL);
;     F.tid = threadIdx.x; F.lane = F.tid & 63; F.wave = __builtin_amdgcn_readfirstlane(F.tid >> 6);
;     F.G = gridDim.x; F.gw = blockIdx.x * NWAVES + F.wave; F.NGW = F.G * NWAVES;
;     volatile LAS unsigned* MISC = (volatile LAS unsigned*)(F.lds + MISC_OFF);
;     for (int u = F.tid; u < (LDS_BYTES - LDSCTL_OFF) / 4; u += NTHR) ((LAS unsigned*)(F.lds + LDSCTL_OFF))[u] = 0u;
;     __syncthreads();
;     if (F.tid < N_INPUTS) { const unsigned long long p = (unsigned long long)args.in[F.tid]; LAS unsigned* t = (LAS unsigned*)(F.lds + PTAB_OFF) + 2 * F.tid; t[0] = (unsigned)p; t[1] = (unsigned)(p >> 32); }
;     __syncthreads();
_Z3fwd4Args:
	s_mov_b32 s101, 0
	s_nop 0
	s_load_dword s48, s[0:1], 0xd0
	s_add_u32 s4, s0, 0xd0
	v_writelane_b32 v255, s0, 0
	s_addc_u32 s5, s1, 0
	v_lshl_add_u32 v1, v0, 2, 0
	v_writelane_b32 v255, s1, 1
	v_writelane_b32 v255, s4, 2
	v_add_u32_e32 v1, 0x20000, v1
	v_mov_b32_e32 v2, 0
	v_readfirstlane_b32 s54, v0
	v_writelane_b32 v255, s5, 3
	ds_write2st64_b32 v1, v2, v2 offset1:8
	ds_write2st64_b32 v1, v2, v2 offset0:16 offset1:24
	v_or_b32_e32 v1, 0x800, v0
	s_mov_b64 s[0:1], -1
	s_and_saveexec_b64 s[4:5], s[0:1]
	v_lshl_add_u32 v3, v1, 2, 0
	v_add_u32_e32 v3, 0x20000, v3
	ds_write_b32 v3, v2
	s_or_b64 exec, exec, s[4:5]
	s_and_saveexec_b64 s[4:5], s[0:1]
	s_add_i32 s0, 0, 0x20000
	v_lshl_add_u32 v1, v1, 2, s0
	v_mov_b32_e32 v2, 0
	ds_write_b32 v1, v2 offset:2048
	s_or_b64 exec, exec, s[4:5]
	v_or_b32_e32 v1, 0xc00, v0
	v_cmp_gt_u32_e64 s[0:1], 7, 6
	v_cmp_gt_u32_e64 s[6:7], 7, 5
	s_and_saveexec_b64 s[4:5], s[6:7]
	v_lshl_add_u32 v2, v1, 2, 0
	v_add_u32_e32 v2, 0x20000, v2
	v_mov_b32_e32 v3, 0
	ds_write_b32 v2, v3
	s_or_b64 exec, exec, s[4:5]
	v_readlane_b32 s4, v255, 0
	v_readlane_b32 s5, v255, 1
	s_load_dwordx2 s[50:51], s[4:5], 0xc0
	s_and_saveexec_b64 s[4:5], s[0:1]
	s_add_i32 s0, 0, 0x20000
	v_lshl_add_u32 v1, v1, 2, s0
	v_mov_b32_e32 v2, 0
	ds_write_b32 v1, v2 offset:2048
	s_or_b64 exec, exec, s[4:5]
	v_cmp_gt_u32_e32 vcc, 23, v0
	s_waitcnt lgkmcnt(0)
	s_barrier
	s_and_saveexec_b64 s[0:1], vcc
	s_cbranch_execz .LBB0_10
	v_readlane_b32 s4, v255, 0
	v_lshlrev_b32_e32 v1, 3, v0
	v_readlane_b32 s5, v255, 1
	s_nop 4
	global_load_dwordx2 v[2:3], v1, s[4:5]
	v_add_u32_e32 v1, 0, v1
	v_add_u32_e32 v1, 0x20200, v1
	s_waitcnt vmcnt(0)
	ds_write_b64 v1, v[2:3]
